# adds RWKV scanner block rewritten: operand prefetch reads in the DPP wait-state slots, sa pair produced in place, one wait per step (33 vs ~40 instructions per step)
# speedup vs baseline: 1.0050x; 1.0050x over previous
.LBB0_512:
	s_and_b64 vcc, exec, s[6:7]
	s_cbranch_vccz .LBB0_482
	s_cmpk_eq_i32 s60, 0x80
	s_cbranch_scc1 .LBB0_483
	s_setprio 2
	s_mul_i32 s7, s60, 0xab
	s_bfe_u32 s7, s7, 0x70009
	s_and_b32 s6, s60, 1
	s_mul_i32 s7, s7, 3
	s_sub_i32 s7, s60, s7
	s_mul_i32 s8, s6, 0x2080
	s_and_b32 s7, s7, 0xff
	s_waitcnt vmcnt(0)
	v_add_u32_e32 v149, s8, v104
	v_lshl_add_u32 v80, s6, 15, v92
	v_lshl_add_u32 v81, s7, 12, v148
	v_lshl_add_u32 v2, s6, 12, v95
	ds_write2_b64 v149, v[70:71], v[72:73] offset1:1
	ds_write2_b32 v149, v74, v75 offset0:65 offset1:66
	ds_write2_b32 v149, v76, v77 offset0:67 offset1:68
	ds_read_b128 v[38:41], v80 offset:0
	ds_read_b128 v[42:45], v80 offset:256
	ds_read_b128 v[46:49], v80 offset:512
	ds_read_b128 v[50:53], v80 offset:768
	ds_read_b64 v[54:55], v81 offset:0
	ds_read_b128 v[56:59], v80 offset:1024
	ds_read_b128 v[150:153], v80 offset:1280
	ds_read_b128 v[154:157], v80 offset:1536
	ds_read_b128 v[158:161], v80 offset:1792
	ds_read_b64 v[60:61], v81 offset:128
	s_waitcnt lgkmcnt(5)
	ds_read_b64 v[78:79], v81 offset:256
	v_pk_mul_f32 v[178:179], v[72:73], v[40:41]
	v_pk_mul_f32 v[180:181], v[76:77], v[40:41]
	v_pk_fma_f32 v[178:179], v[70:71], v[38:39], v[178:179]
	v_pk_fma_f32 v[180:181], v[74:75], v[38:39], v[180:181]
	v_add_f32_e32 v182, v178, v179
	v_add_f32_e32 v183, v180, v181
	ds_read_b128 v[162:165], v80 offset:2048
	v_add_f32_dpp v182, v182, v182 row_ror:8 row_mask:0xf bank_mask:0xf bound_ctrl:1
	v_add_f32_dpp v183, v183, v183 row_ror:8 row_mask:0xf bank_mask:0xf bound_ctrl:1
	ds_read_b128 v[166:169], v80 offset:2304
	v_add_f32_dpp v182, v182, v182 row_ror:4 row_mask:0xf bank_mask:0xf bound_ctrl:1
	v_add_f32_dpp v183, v183, v183 row_ror:4 row_mask:0xf bank_mask:0xf bound_ctrl:1
	ds_read_b128 v[170:173], v80 offset:2560
	v_add_f32_dpp v182, v182, v182 row_ror:2 row_mask:0xf bank_mask:0xf bound_ctrl:1
	v_add_f32_dpp v183, v183, v183 row_ror:2 row_mask:0xf bank_mask:0xf bound_ctrl:1
	ds_read_b128 v[174:177], v80 offset:2816
	v_add_f32_dpp v182, v182, v182 row_ror:1 row_mask:0xf bank_mask:0xf bound_ctrl:1
	v_add_f32_dpp v183, v183, v183 row_ror:1 row_mask:0xf bank_mask:0xf bound_ctrl:1
	v_pk_mul_f32 v[240:241], v[46:47], v[182:183] op_sel_hi:[1,0]
	v_pk_mul_f32 v[242:243], v[48:49], v[182:183] op_sel_hi:[1,0]
	v_pk_mul_f32 v[244:245], v[46:47], v[182:183] op_sel:[0,1]
	v_pk_mul_f32 v[246:247], v[48:49], v[182:183] op_sel:[0,1]
	ds_write_b64 v2, v[182:183] offset:0
	v_pk_fma_f32 v[72:73], v[72:73], v[44:45], v[242:243]
	v_pk_fma_f32 v[76:77], v[76:77], v[44:45], v[246:247]
	v_pk_fma_f32 v[70:71], v[70:71], v[42:43], v[240:241]
	v_pk_fma_f32 v[74:75], v[74:75], v[42:43], v[244:245]
	v_pk_fma_f32 v[72:73], v[52:53], v[54:55], v[72:73] op_sel_hi:[1,0,1]
	v_pk_fma_f32 v[76:77], v[52:53], v[54:55], v[76:77] op_sel:[0,1,0]
	v_pk_fma_f32 v[70:71], v[50:51], v[54:55], v[70:71] op_sel_hi:[1,0,1]
	v_pk_fma_f32 v[74:75], v[50:51], v[54:55], v[74:75] op_sel:[0,1,0]
	s_waitcnt lgkmcnt(6)
	ds_read_b64 v[54:55], v81 offset:384
	v_pk_mul_f32 v[178:179], v[72:73], v[58:59]
	v_pk_mul_f32 v[180:181], v[76:77], v[58:59]
	v_pk_fma_f32 v[178:179], v[70:71], v[56:57], v[178:179]
	v_pk_fma_f32 v[180:181], v[74:75], v[56:57], v[180:181]
	v_add_f32_e32 v184, v178, v179
	v_add_f32_e32 v185, v180, v181
	ds_read_b128 v[38:41], v80 offset:3072
	v_add_f32_dpp v184, v184, v184 row_ror:8 row_mask:0xf bank_mask:0xf bound_ctrl:1
	v_add_f32_dpp v185, v185, v185 row_ror:8 row_mask:0xf bank_mask:0xf bound_ctrl:1
	ds_read_b128 v[42:45], v80 offset:3328
	v_add_f32_dpp v184, v184, v184 row_ror:4 row_mask:0xf bank_mask:0xf bound_ctrl:1
	v_add_f32_dpp v185, v185, v185 row_ror:4 row_mask:0xf bank_mask:0xf bound_ctrl:1
	ds_read_b128 v[46:49], v80 offset:3584
	v_add_f32_dpp v184, v184, v184 row_ror:2 row_mask:0xf bank_mask:0xf bound_ctrl:1
	v_add_f32_dpp v185, v185, v185 row_ror:2 row_mask:0xf bank_mask:0xf bound_ctrl:1
	ds_read_b128 v[50:53], v80 offset:3840
	v_add_f32_dpp v184, v184, v184 row_ror:1 row_mask:0xf bank_mask:0xf bound_ctrl:1
	v_add_f32_dpp v185, v185, v185 row_ror:1 row_mask:0xf bank_mask:0xf bound_ctrl:1
	v_pk_mul_f32 v[240:241], v[154:155], v[184:185] op_sel_hi:[1,0]
	v_pk_mul_f32 v[242:243], v[156:157], v[184:185] op_sel_hi:[1,0]
	v_pk_mul_f32 v[244:245], v[154:155], v[184:185] op_sel:[0,1]
	v_pk_mul_f32 v[246:247], v[156:157], v[184:185] op_sel:[0,1]
	ds_write_b64 v2, v[184:185] offset:128
	v_pk_fma_f32 v[72:73], v[72:73], v[152:153], v[242:243]
	v_pk_fma_f32 v[76:77], v[76:77], v[152:153], v[246:247]
	v_pk_fma_f32 v[70:71], v[70:71], v[150:151], v[240:241]
	v_pk_fma_f32 v[74:75], v[74:75], v[150:151], v[244:245]
	v_pk_fma_f32 v[72:73], v[160:161], v[60:61], v[72:73] op_sel_hi:[1,0,1]
	v_pk_fma_f32 v[76:77], v[160:161], v[60:61], v[76:77] op_sel:[0,1,0]
	v_pk_fma_f32 v[70:71], v[158:159], v[60:61], v[70:71] op_sel_hi:[1,0,1]
	v_pk_fma_f32 v[74:75], v[158:159], v[60:61], v[74:75] op_sel:[0,1,0]
	s_waitcnt lgkmcnt(7)
	ds_read_b64 v[60:61], v81 offset:512
	v_pk_mul_f32 v[178:179], v[72:73], v[164:165]
	v_pk_mul_f32 v[180:181], v[76:77], v[164:165]
	v_pk_fma_f32 v[178:179], v[70:71], v[162:163], v[178:179]
	v_pk_fma_f32 v[180:181], v[74:75], v[162:163], v[180:181]
	v_add_f32_e32 v182, v178, v179
	v_add_f32_e32 v183, v180, v181
	ds_read_b128 v[56:59], v80 offset:4096
	v_add_f32_dpp v182, v182, v182 row_ror:8 row_mask:0xf bank_mask:0xf bound_ctrl:1
	v_add_f32_dpp v183, v183, v183 row_ror:8 row_mask:0xf bank_mask:0xf bound_ctrl:1
	ds_read_b128 v[150:153], v80 offset:4352
	v_add_f32_dpp v182, v182, v182 row_ror:4 row_mask:0xf bank_mask:0xf bound_ctrl:1
	v_add_f32_dpp v183, v183, v183 row_ror:4 row_mask:0xf bank_mask:0xf bound_ctrl:1
	ds_read_b128 v[154:157], v80 offset:4608
	v_add_f32_dpp v182, v182, v182 row_ror:2 row_mask:0xf bank_mask:0xf bound_ctrl:1
	v_add_f32_dpp v183, v183, v183 row_ror:2 row_mask:0xf bank_mask:0xf bound_ctrl:1
	ds_read_b128 v[158:161], v80 offset:4864
	v_add_f32_dpp v182, v182, v182 row_ror:1 row_mask:0xf bank_mask:0xf bound_ctrl:1
	v_add_f32_dpp v183, v183, v183 row_ror:1 row_mask:0xf bank_mask:0xf bound_ctrl:1
	v_pk_mul_f32 v[240:241], v[170:171], v[182:183] op_sel_hi:[1,0]
	v_pk_mul_f32 v[242:243], v[172:173], v[182:183] op_sel_hi:[1,0]
	v_pk_mul_f32 v[244:245], v[170:171], v[182:183] op_sel:[0,1]
	v_pk_mul_f32 v[246:247], v[172:173], v[182:183] op_sel:[0,1]
	ds_write_b64 v2, v[182:183] offset:256
	v_pk_fma_f32 v[72:73], v[72:73], v[168:169], v[242:243]
	v_pk_fma_f32 v[76:77], v[76:77], v[168:169], v[246:247]
	v_pk_fma_f32 v[70:71], v[70:71], v[166:167], v[240:241]
	v_pk_fma_f32 v[74:75], v[74:75], v[166:167], v[244:245]
	v_pk_fma_f32 v[72:73], v[176:177], v[78:79], v[72:73] op_sel_hi:[1,0,1]
	v_pk_fma_f32 v[76:77], v[176:177], v[78:79], v[76:77] op_sel:[0,1,0]
	v_pk_fma_f32 v[70:71], v[174:175], v[78:79], v[70:71] op_sel_hi:[1,0,1]
	v_pk_fma_f32 v[74:75], v[174:175], v[78:79], v[74:75] op_sel:[0,1,0]
	s_waitcnt lgkmcnt(7)
	ds_read_b64 v[78:79], v81 offset:640
	v_pk_mul_f32 v[178:179], v[72:73], v[40:41]
	v_pk_mul_f32 v[180:181], v[76:77], v[40:41]
	v_pk_fma_f32 v[178:179], v[70:71], v[38:39], v[178:179]
	v_pk_fma_f32 v[180:181], v[74:75], v[38:39], v[180:181]
	v_add_f32_e32 v184, v178, v179
	v_add_f32_e32 v185, v180, v181
	ds_read_b128 v[162:165], v80 offset:5120
	v_add_f32_dpp v184, v184, v184 row_ror:8 row_mask:0xf bank_mask:0xf bound_ctrl:1
	v_add_f32_dpp v185, v185, v185 row_ror:8 row_mask:0xf bank_mask:0xf bound_ctrl:1
	ds_read_b128 v[166:169], v80 offset:5376
	v_add_f32_dpp v184, v184, v184 row_ror:4 row_mask:0xf bank_mask:0xf bound_ctrl:1
	v_add_f32_dpp v185, v185, v185 row_ror:4 row_mask:0xf bank_mask:0xf bound_ctrl:1
	ds_read_b128 v[170:173], v80 offset:5632
	v_add_f32_dpp v184, v184, v184 row_ror:2 row_mask:0xf bank_mask:0xf bound_ctrl:1
	v_add_f32_dpp v185, v185, v185 row_ror:2 row_mask:0xf bank_mask:0xf bound_ctrl:1
	ds_read_b128 v[174:177], v80 offset:5888
	v_add_f32_dpp v184, v184, v184 row_ror:1 row_mask:0xf bank_mask:0xf bound_ctrl:1
	v_add_f32_dpp v185, v185, v185 row_ror:1 row_mask:0xf bank_mask:0xf bound_ctrl:1
	v_pk_mul_f32 v[240:241], v[46:47], v[184:185] op_sel_hi:[1,0]
	v_pk_mul_f32 v[242:243], v[48:49], v[184:185] op_sel_hi:[1,0]
	v_pk_mul_f32 v[244:245], v[46:47], v[184:185] op_sel:[0,1]
	v_pk_mul_f32 v[246:247], v[48:49], v[184:185] op_sel:[0,1]
	ds_write_b64 v2, v[184:185] offset:384
	v_pk_fma_f32 v[72:73], v[72:73], v[44:45], v[242:243]
	v_pk_fma_f32 v[76:77], v[76:77], v[44:45], v[246:247]
	v_pk_fma_f32 v[70:71], v[70:71], v[42:43], v[240:241]
	v_pk_fma_f32 v[74:75], v[74:75], v[42:43], v[244:245]
	v_pk_fma_f32 v[72:73], v[52:53], v[54:55], v[72:73] op_sel_hi:[1,0,1]
	v_pk_fma_f32 v[76:77], v[52:53], v[54:55], v[76:77] op_sel:[0,1,0]
	v_pk_fma_f32 v[70:71], v[50:51], v[54:55], v[70:71] op_sel_hi:[1,0,1]
	v_pk_fma_f32 v[74:75], v[50:51], v[54:55], v[74:75] op_sel:[0,1,0]
	s_waitcnt lgkmcnt(7)
	ds_read_b64 v[54:55], v81 offset:768
	v_pk_mul_f32 v[178:179], v[72:73], v[58:59]
	v_pk_mul_f32 v[180:181], v[76:77], v[58:59]
	v_pk_fma_f32 v[178:179], v[70:71], v[56:57], v[178:179]
	v_pk_fma_f32 v[180:181], v[74:75], v[56:57], v[180:181]
	v_add_f32_e32 v182, v178, v179
	v_add_f32_e32 v183, v180, v181
	ds_read_b128 v[38:41], v80 offset:6144
	v_add_f32_dpp v182, v182, v182 row_ror:8 row_mask:0xf bank_mask:0xf bound_ctrl:1
	v_add_f32_dpp v183, v183, v183 row_ror:8 row_mask:0xf bank_mask:0xf bound_ctrl:1
	ds_read_b128 v[42:45], v80 offset:6400
	v_add_f32_dpp v182, v182, v182 row_ror:4 row_mask:0xf bank_mask:0xf bound_ctrl:1
	v_add_f32_dpp v183, v183, v183 row_ror:4 row_mask:0xf bank_mask:0xf bound_ctrl:1
	ds_read_b128 v[46:49], v80 offset:6656
	v_add_f32_dpp v182, v182, v182 row_ror:2 row_mask:0xf bank_mask:0xf bound_ctrl:1
	v_add_f32_dpp v183, v183, v183 row_ror:2 row_mask:0xf bank_mask:0xf bound_ctrl:1
	ds_read_b128 v[50:53], v80 offset:6912
	v_add_f32_dpp v182, v182, v182 row_ror:1 row_mask:0xf bank_mask:0xf bound_ctrl:1
	v_add_f32_dpp v183, v183, v183 row_ror:1 row_mask:0xf bank_mask:0xf bound_ctrl:1
	v_pk_mul_f32 v[240:241], v[154:155], v[182:183] op_sel_hi:[1,0]
	v_pk_mul_f32 v[242:243], v[156:157], v[182:183] op_sel_hi:[1,0]
	v_pk_mul_f32 v[244:245], v[154:155], v[182:183] op_sel:[0,1]
	v_pk_mul_f32 v[246:247], v[156:157], v[182:183] op_sel:[0,1]
	ds_write_b64 v2, v[182:183] offset:512
	v_pk_fma_f32 v[72:73], v[72:73], v[152:153], v[242:243]
	v_pk_fma_f32 v[76:77], v[76:77], v[152:153], v[246:247]
	v_pk_fma_f32 v[70:71], v[70:71], v[150:151], v[240:241]
	v_pk_fma_f32 v[74:75], v[74:75], v[150:151], v[244:245]
	v_pk_fma_f32 v[72:73], v[160:161], v[60:61], v[72:73] op_sel_hi:[1,0,1]
	v_pk_fma_f32 v[76:77], v[160:161], v[60:61], v[76:77] op_sel:[0,1,0]
	v_pk_fma_f32 v[70:71], v[158:159], v[60:61], v[70:71] op_sel_hi:[1,0,1]
	v_pk_fma_f32 v[74:75], v[158:159], v[60:61], v[74:75] op_sel:[0,1,0]
	s_waitcnt lgkmcnt(7)
	ds_read_b64 v[60:61], v81 offset:896
	v_pk_mul_f32 v[178:179], v[72:73], v[164:165]
	v_pk_mul_f32 v[180:181], v[76:77], v[164:165]
	v_pk_fma_f32 v[178:179], v[70:71], v[162:163], v[178:179]
	v_pk_fma_f32 v[180:181], v[74:75], v[162:163], v[180:181]
	v_add_f32_e32 v184, v178, v179
	v_add_f32_e32 v185, v180, v181
	ds_read_b128 v[56:59], v80 offset:7168
	v_add_f32_dpp v184, v184, v184 row_ror:8 row_mask:0xf bank_mask:0xf bound_ctrl:1
	v_add_f32_dpp v185, v185, v185 row_ror:8 row_mask:0xf bank_mask:0xf bound_ctrl:1
	ds_read_b128 v[150:153], v80 offset:7424
	v_add_f32_dpp v184, v184, v184 row_ror:4 row_mask:0xf bank_mask:0xf bound_ctrl:1
	v_add_f32_dpp v185, v185, v185 row_ror:4 row_mask:0xf bank_mask:0xf bound_ctrl:1
	ds_read_b128 v[154:157], v80 offset:7680
	v_add_f32_dpp v184, v184, v184 row_ror:2 row_mask:0xf bank_mask:0xf bound_ctrl:1
	v_add_f32_dpp v185, v185, v185 row_ror:2 row_mask:0xf bank_mask:0xf bound_ctrl:1
	ds_read_b128 v[158:161], v80 offset:7936
	v_add_f32_dpp v184, v184, v184 row_ror:1 row_mask:0xf bank_mask:0xf bound_ctrl:1
	v_add_f32_dpp v185, v185, v185 row_ror:1 row_mask:0xf bank_mask:0xf bound_ctrl:1
	v_pk_mul_f32 v[240:241], v[170:171], v[184:185] op_sel_hi:[1,0]
	v_pk_mul_f32 v[242:243], v[172:173], v[184:185] op_sel_hi:[1,0]
	v_pk_mul_f32 v[244:245], v[170:171], v[184:185] op_sel:[0,1]
	v_pk_mul_f32 v[246:247], v[172:173], v[184:185] op_sel:[0,1]
	ds_write_b64 v2, v[184:185] offset:640
	v_pk_fma_f32 v[72:73], v[72:73], v[168:169], v[242:243]
	v_pk_fma_f32 v[76:77], v[76:77], v[168:169], v[246:247]
	v_pk_fma_f32 v[70:71], v[70:71], v[166:167], v[240:241]
	v_pk_fma_f32 v[74:75], v[74:75], v[166:167], v[244:245]
	v_pk_fma_f32 v[72:73], v[176:177], v[78:79], v[72:73] op_sel_hi:[1,0,1]
	v_pk_fma_f32 v[76:77], v[176:177], v[78:79], v[76:77] op_sel:[0,1,0]
	v_pk_fma_f32 v[70:71], v[174:175], v[78:79], v[70:71] op_sel_hi:[1,0,1]
	v_pk_fma_f32 v[74:75], v[174:175], v[78:79], v[74:75] op_sel:[0,1,0]
	s_waitcnt lgkmcnt(7)
	ds_read_b64 v[78:79], v81 offset:1024
	v_pk_mul_f32 v[178:179], v[72:73], v[40:41]
	v_pk_mul_f32 v[180:181], v[76:77], v[40:41]
	v_pk_fma_f32 v[178:179], v[70:71], v[38:39], v[178:179]
	v_pk_fma_f32 v[180:181], v[74:75], v[38:39], v[180:181]
	v_add_f32_e32 v182, v178, v179
	v_add_f32_e32 v183, v180, v181
	ds_read_b128 v[162:165], v80 offset:8192
	v_add_f32_dpp v182, v182, v182 row_ror:8 row_mask:0xf bank_mask:0xf bound_ctrl:1
	v_add_f32_dpp v183, v183, v183 row_ror:8 row_mask:0xf bank_mask:0xf bound_ctrl:1
	ds_read_b128 v[166:169], v80 offset:8448
	v_add_f32_dpp v182, v182, v182 row_ror:4 row_mask:0xf bank_mask:0xf bound_ctrl:1
	v_add_f32_dpp v183, v183, v183 row_ror:4 row_mask:0xf bank_mask:0xf bound_ctrl:1
	ds_read_b128 v[170:173], v80 offset:8704
	v_add_f32_dpp v182, v182, v182 row_ror:2 row_mask:0xf bank_mask:0xf bound_ctrl:1
	v_add_f32_dpp v183, v183, v183 row_ror:2 row_mask:0xf bank_mask:0xf bound_ctrl:1
	ds_read_b128 v[174:177], v80 offset:8960
	v_add_f32_dpp v182, v182, v182 row_ror:1 row_mask:0xf bank_mask:0xf bound_ctrl:1
	v_add_f32_dpp v183, v183, v183 row_ror:1 row_mask:0xf bank_mask:0xf bound_ctrl:1
	v_pk_mul_f32 v[240:241], v[46:47], v[182:183] op_sel_hi:[1,0]
	v_pk_mul_f32 v[242:243], v[48:49], v[182:183] op_sel_hi:[1,0]
	v_pk_mul_f32 v[244:245], v[46:47], v[182:183] op_sel:[0,1]
	v_pk_mul_f32 v[246:247], v[48:49], v[182:183] op_sel:[0,1]
	ds_write_b64 v2, v[182:183] offset:768
	v_pk_fma_f32 v[72:73], v[72:73], v[44:45], v[242:243]
	v_pk_fma_f32 v[76:77], v[76:77], v[44:45], v[246:247]
	v_pk_fma_f32 v[70:71], v[70:71], v[42:43], v[240:241]
	v_pk_fma_f32 v[74:75], v[74:75], v[42:43], v[244:245]
	v_pk_fma_f32 v[72:73], v[52:53], v[54:55], v[72:73] op_sel_hi:[1,0,1]
	v_pk_fma_f32 v[76:77], v[52:53], v[54:55], v[76:77] op_sel:[0,1,0]
	v_pk_fma_f32 v[70:71], v[50:51], v[54:55], v[70:71] op_sel_hi:[1,0,1]
	v_pk_fma_f32 v[74:75], v[50:51], v[54:55], v[74:75] op_sel:[0,1,0]
	s_waitcnt lgkmcnt(7)
	ds_read_b64 v[54:55], v81 offset:1152
	v_pk_mul_f32 v[178:179], v[72:73], v[58:59]
	v_pk_mul_f32 v[180:181], v[76:77], v[58:59]
	v_pk_fma_f32 v[178:179], v[70:71], v[56:57], v[178:179]
	v_pk_fma_f32 v[180:181], v[74:75], v[56:57], v[180:181]
	v_add_f32_e32 v184, v178, v179
	v_add_f32_e32 v185, v180, v181
	ds_read_b128 v[38:41], v80 offset:9216
	v_add_f32_dpp v184, v184, v184 row_ror:8 row_mask:0xf bank_mask:0xf bound_ctrl:1
	v_add_f32_dpp v185, v185, v185 row_ror:8 row_mask:0xf bank_mask:0xf bound_ctrl:1
	ds_read_b128 v[42:45], v80 offset:9472
	v_add_f32_dpp v184, v184, v184 row_ror:4 row_mask:0xf bank_mask:0xf bound_ctrl:1
	v_add_f32_dpp v185, v185, v185 row_ror:4 row_mask:0xf bank_mask:0xf bound_ctrl:1
	ds_read_b128 v[46:49], v80 offset:9728
	v_add_f32_dpp v184, v184, v184 row_ror:2 row_mask:0xf bank_mask:0xf bound_ctrl:1
	v_add_f32_dpp v185, v185, v185 row_ror:2 row_mask:0xf bank_mask:0xf bound_ctrl:1
	ds_read_b128 v[50:53], v80 offset:9984
	v_add_f32_dpp v184, v184, v184 row_ror:1 row_mask:0xf bank_mask:0xf bound_ctrl:1
	v_add_f32_dpp v185, v185, v185 row_ror:1 row_mask:0xf bank_mask:0xf bound_ctrl:1
	v_pk_mul_f32 v[240:241], v[154:155], v[184:185] op_sel_hi:[1,0]
	v_pk_mul_f32 v[242:243], v[156:157], v[184:185] op_sel_hi:[1,0]
	v_pk_mul_f32 v[244:245], v[154:155], v[184:185] op_sel:[0,1]
	v_pk_mul_f32 v[246:247], v[156:157], v[184:185] op_sel:[0,1]
	ds_write_b64 v2, v[184:185] offset:896
	v_pk_fma_f32 v[72:73], v[72:73], v[152:153], v[242:243]
	v_pk_fma_f32 v[76:77], v[76:77], v[152:153], v[246:247]
	v_pk_fma_f32 v[70:71], v[70:71], v[150:151], v[240:241]
	v_pk_fma_f32 v[74:75], v[74:75], v[150:151], v[244:245]
	v_pk_fma_f32 v[72:73], v[160:161], v[60:61], v[72:73] op_sel_hi:[1,0,1]
	v_pk_fma_f32 v[76:77], v[160:161], v[60:61], v[76:77] op_sel:[0,1,0]
	v_pk_fma_f32 v[70:71], v[158:159], v[60:61], v[70:71] op_sel_hi:[1,0,1]
	v_pk_fma_f32 v[74:75], v[158:159], v[60:61], v[74:75] op_sel:[0,1,0]
	s_waitcnt lgkmcnt(7)
	ds_read_b64 v[60:61], v81 offset:1280
	v_pk_mul_f32 v[178:179], v[72:73], v[164:165]
	v_pk_mul_f32 v[180:181], v[76:77], v[164:165]
	v_pk_fma_f32 v[178:179], v[70:71], v[162:163], v[178:179]
	v_pk_fma_f32 v[180:181], v[74:75], v[162:163], v[180:181]
	v_add_f32_e32 v182, v178, v179
	v_add_f32_e32 v183, v180, v181
	ds_read_b128 v[56:59], v80 offset:10240
	v_add_f32_dpp v182, v182, v182 row_ror:8 row_mask:0xf bank_mask:0xf bound_ctrl:1
	v_add_f32_dpp v183, v183, v183 row_ror:8 row_mask:0xf bank_mask:0xf bound_ctrl:1
	ds_read_b128 v[150:153], v80 offset:10496
	v_add_f32_dpp v182, v182, v182 row_ror:4 row_mask:0xf bank_mask:0xf bound_ctrl:1
	v_add_f32_dpp v183, v183, v183 row_ror:4 row_mask:0xf bank_mask:0xf bound_ctrl:1
	ds_read_b128 v[154:157], v80 offset:10752
	v_add_f32_dpp v182, v182, v182 row_ror:2 row_mask:0xf bank_mask:0xf bound_ctrl:1
	v_add_f32_dpp v183, v183, v183 row_ror:2 row_mask:0xf bank_mask:0xf bound_ctrl:1
	ds_read_b128 v[158:161], v80 offset:11008
	v_add_f32_dpp v182, v182, v182 row_ror:1 row_mask:0xf bank_mask:0xf bound_ctrl:1
	v_add_f32_dpp v183, v183, v183 row_ror:1 row_mask:0xf bank_mask:0xf bound_ctrl:1
	v_pk_mul_f32 v[240:241], v[170:171], v[182:183] op_sel_hi:[1,0]
	v_pk_mul_f32 v[242:243], v[172:173], v[182:183] op_sel_hi:[1,0]
	v_pk_mul_f32 v[244:245], v[170:171], v[182:183] op_sel:[0,1]
	v_pk_mul_f32 v[246:247], v[172:173], v[182:183] op_sel:[0,1]
	ds_write_b64 v2, v[182:183] offset:1024
	v_pk_fma_f32 v[72:73], v[72:73], v[168:169], v[242:243]
	v_pk_fma_f32 v[76:77], v[76:77], v[168:169], v[246:247]
	v_pk_fma_f32 v[70:71], v[70:71], v[166:167], v[240:241]
	v_pk_fma_f32 v[74:75], v[74:75], v[166:167], v[244:245]
	v_pk_fma_f32 v[72:73], v[176:177], v[78:79], v[72:73] op_sel_hi:[1,0,1]
	v_pk_fma_f32 v[76:77], v[176:177], v[78:79], v[76:77] op_sel:[0,1,0]
	v_pk_fma_f32 v[70:71], v[174:175], v[78:79], v[70:71] op_sel_hi:[1,0,1]
	v_pk_fma_f32 v[74:75], v[174:175], v[78:79], v[74:75] op_sel:[0,1,0]
	s_waitcnt lgkmcnt(7)
	ds_read_b64 v[78:79], v81 offset:1408
	v_pk_mul_f32 v[178:179], v[72:73], v[40:41]
	v_pk_mul_f32 v[180:181], v[76:77], v[40:41]
	v_pk_fma_f32 v[178:179], v[70:71], v[38:39], v[178:179]
	v_pk_fma_f32 v[180:181], v[74:75], v[38:39], v[180:181]
	v_add_f32_e32 v184, v178, v179
	v_add_f32_e32 v185, v180, v181
	ds_read_b128 v[162:165], v80 offset:11264
	v_add_f32_dpp v184, v184, v184 row_ror:8 row_mask:0xf bank_mask:0xf bound_ctrl:1
	v_add_f32_dpp v185, v185, v185 row_ror:8 row_mask:0xf bank_mask:0xf bound_ctrl:1
	ds_read_b128 v[166:169], v80 offset:11520
	v_add_f32_dpp v184, v184, v184 row_ror:4 row_mask:0xf bank_mask:0xf bound_ctrl:1
	v_add_f32_dpp v185, v185, v185 row_ror:4 row_mask:0xf bank_mask:0xf bound_ctrl:1
	ds_read_b128 v[170:173], v80 offset:11776
	v_add_f32_dpp v184, v184, v184 row_ror:2 row_mask:0xf bank_mask:0xf bound_ctrl:1
	v_add_f32_dpp v185, v185, v185 row_ror:2 row_mask:0xf bank_mask:0xf bound_ctrl:1
	ds_read_b128 v[174:177], v80 offset:12032
	v_add_f32_dpp v184, v184, v184 row_ror:1 row_mask:0xf bank_mask:0xf bound_ctrl:1
	v_add_f32_dpp v185, v185, v185 row_ror:1 row_mask:0xf bank_mask:0xf bound_ctrl:1
	v_pk_mul_f32 v[240:241], v[46:47], v[184:185] op_sel_hi:[1,0]
	v_pk_mul_f32 v[242:243], v[48:49], v[184:185] op_sel_hi:[1,0]
	v_pk_mul_f32 v[244:245], v[46:47], v[184:185] op_sel:[0,1]
	v_pk_mul_f32 v[246:247], v[48:49], v[184:185] op_sel:[0,1]
	ds_write_b64 v2, v[184:185] offset:1152
	v_pk_fma_f32 v[72:73], v[72:73], v[44:45], v[242:243]
	v_pk_fma_f32 v[76:77], v[76:77], v[44:45], v[246:247]
	v_pk_fma_f32 v[70:71], v[70:71], v[42:43], v[240:241]
	v_pk_fma_f32 v[74:75], v[74:75], v[42:43], v[244:245]
	v_pk_fma_f32 v[72:73], v[52:53], v[54:55], v[72:73] op_sel_hi:[1,0,1]
	v_pk_fma_f32 v[76:77], v[52:53], v[54:55], v[76:77] op_sel:[0,1,0]
	v_pk_fma_f32 v[70:71], v[50:51], v[54:55], v[70:71] op_sel_hi:[1,0,1]
	v_pk_fma_f32 v[74:75], v[50:51], v[54:55], v[74:75] op_sel:[0,1,0]
	s_waitcnt lgkmcnt(7)
	ds_read_b64 v[54:55], v81 offset:1536
	v_pk_mul_f32 v[178:179], v[72:73], v[58:59]
	v_pk_mul_f32 v[180:181], v[76:77], v[58:59]
	v_pk_fma_f32 v[178:179], v[70:71], v[56:57], v[178:179]
	v_pk_fma_f32 v[180:181], v[74:75], v[56:57], v[180:181]
	v_add_f32_e32 v182, v178, v179
	v_add_f32_e32 v183, v180, v181
	ds_read_b128 v[38:41], v80 offset:12288
	v_add_f32_dpp v182, v182, v182 row_ror:8 row_mask:0xf bank_mask:0xf bound_ctrl:1
	v_add_f32_dpp v183, v183, v183 row_ror:8 row_mask:0xf bank_mask:0xf bound_ctrl:1
	ds_read_b128 v[42:45], v80 offset:12544
	v_add_f32_dpp v182, v182, v182 row_ror:4 row_mask:0xf bank_mask:0xf bound_ctrl:1
	v_add_f32_dpp v183, v183, v183 row_ror:4 row_mask:0xf bank_mask:0xf bound_ctrl:1
	ds_read_b128 v[46:49], v80 offset:12800
	v_add_f32_dpp v182, v182, v182 row_ror:2 row_mask:0xf bank_mask:0xf bound_ctrl:1
	v_add_f32_dpp v183, v183, v183 row_ror:2 row_mask:0xf bank_mask:0xf bound_ctrl:1
	ds_read_b128 v[50:53], v80 offset:13056
	v_add_f32_dpp v182, v182, v182 row_ror:1 row_mask:0xf bank_mask:0xf bound_ctrl:1
	v_add_f32_dpp v183, v183, v183 row_ror:1 row_mask:0xf bank_mask:0xf bound_ctrl:1
	v_pk_mul_f32 v[240:241], v[154:155], v[182:183] op_sel_hi:[1,0]
	v_pk_mul_f32 v[242:243], v[156:157], v[182:183] op_sel_hi:[1,0]
	v_pk_mul_f32 v[244:245], v[154:155], v[182:183] op_sel:[0,1]
	v_pk_mul_f32 v[246:247], v[156:157], v[182:183] op_sel:[0,1]
	ds_write_b64 v2, v[182:183] offset:1280
	v_pk_fma_f32 v[72:73], v[72:73], v[152:153], v[242:243]
	v_pk_fma_f32 v[76:77], v[76:77], v[152:153], v[246:247]
	v_pk_fma_f32 v[70:71], v[70:71], v[150:151], v[240:241]
	v_pk_fma_f32 v[74:75], v[74:75], v[150:151], v[244:245]
	v_pk_fma_f32 v[72:73], v[160:161], v[60:61], v[72:73] op_sel_hi:[1,0,1]
	v_pk_fma_f32 v[76:77], v[160:161], v[60:61], v[76:77] op_sel:[0,1,0]
	v_pk_fma_f32 v[70:71], v[158:159], v[60:61], v[70:71] op_sel_hi:[1,0,1]
	v_pk_fma_f32 v[74:75], v[158:159], v[60:61], v[74:75] op_sel:[0,1,0]
	s_waitcnt lgkmcnt(7)
	ds_read_b64 v[60:61], v81 offset:1664
	v_pk_mul_f32 v[178:179], v[72:73], v[164:165]
	v_pk_mul_f32 v[180:181], v[76:77], v[164:165]
	v_pk_fma_f32 v[178:179], v[70:71], v[162:163], v[178:179]
	v_pk_fma_f32 v[180:181], v[74:75], v[162:163], v[180:181]
	v_add_f32_e32 v184, v178, v179
	v_add_f32_e32 v185, v180, v181
	ds_read_b128 v[56:59], v80 offset:13312
	v_add_f32_dpp v184, v184, v184 row_ror:8 row_mask:0xf bank_mask:0xf bound_ctrl:1
	v_add_f32_dpp v185, v185, v185 row_ror:8 row_mask:0xf bank_mask:0xf bound_ctrl:1
	ds_read_b128 v[150:153], v80 offset:13568
	v_add_f32_dpp v184, v184, v184 row_ror:4 row_mask:0xf bank_mask:0xf bound_ctrl:1
	v_add_f32_dpp v185, v185, v185 row_ror:4 row_mask:0xf bank_mask:0xf bound_ctrl:1
	ds_read_b128 v[154:157], v80 offset:13824
	v_add_f32_dpp v184, v184, v184 row_ror:2 row_mask:0xf bank_mask:0xf bound_ctrl:1
	v_add_f32_dpp v185, v185, v185 row_ror:2 row_mask:0xf bank_mask:0xf bound_ctrl:1
	ds_read_b128 v[158:161], v80 offset:14080
	v_add_f32_dpp v184, v184, v184 row_ror:1 row_mask:0xf bank_mask:0xf bound_ctrl:1
	v_add_f32_dpp v185, v185, v185 row_ror:1 row_mask:0xf bank_mask:0xf bound_ctrl:1
	v_pk_mul_f32 v[240:241], v[170:171], v[184:185] op_sel_hi:[1,0]
	v_pk_mul_f32 v[242:243], v[172:173], v[184:185] op_sel_hi:[1,0]
	v_pk_mul_f32 v[244:245], v[170:171], v[184:185] op_sel:[0,1]
	v_pk_mul_f32 v[246:247], v[172:173], v[184:185] op_sel:[0,1]
	ds_write_b64 v2, v[184:185] offset:1408
	v_pk_fma_f32 v[72:73], v[72:73], v[168:169], v[242:243]
	v_pk_fma_f32 v[76:77], v[76:77], v[168:169], v[246:247]
	v_pk_fma_f32 v[70:71], v[70:71], v[166:167], v[240:241]
	v_pk_fma_f32 v[74:75], v[74:75], v[166:167], v[244:245]
	v_pk_fma_f32 v[72:73], v[176:177], v[78:79], v[72:73] op_sel_hi:[1,0,1]
	v_pk_fma_f32 v[76:77], v[176:177], v[78:79], v[76:77] op_sel:[0,1,0]
	v_pk_fma_f32 v[70:71], v[174:175], v[78:79], v[70:71] op_sel_hi:[1,0,1]
	v_pk_fma_f32 v[74:75], v[174:175], v[78:79], v[74:75] op_sel:[0,1,0]
	s_waitcnt lgkmcnt(7)
	ds_read_b64 v[78:79], v81 offset:1792
	v_pk_mul_f32 v[178:179], v[72:73], v[40:41]
	v_pk_mul_f32 v[180:181], v[76:77], v[40:41]
	v_pk_fma_f32 v[178:179], v[70:71], v[38:39], v[178:179]
	v_pk_fma_f32 v[180:181], v[74:75], v[38:39], v[180:181]
	v_add_f32_e32 v182, v178, v179
	v_add_f32_e32 v183, v180, v181
	ds_read_b128 v[162:165], v80 offset:14336
	v_add_f32_dpp v182, v182, v182 row_ror:8 row_mask:0xf bank_mask:0xf bound_ctrl:1
	v_add_f32_dpp v183, v183, v183 row_ror:8 row_mask:0xf bank_mask:0xf bound_ctrl:1
	ds_read_b128 v[166:169], v80 offset:14592
	v_add_f32_dpp v182, v182, v182 row_ror:4 row_mask:0xf bank_mask:0xf bound_ctrl:1
	v_add_f32_dpp v183, v183, v183 row_ror:4 row_mask:0xf bank_mask:0xf bound_ctrl:1
	ds_read_b128 v[170:173], v80 offset:14848
	v_add_f32_dpp v182, v182, v182 row_ror:2 row_mask:0xf bank_mask:0xf bound_ctrl:1
	v_add_f32_dpp v183, v183, v183 row_ror:2 row_mask:0xf bank_mask:0xf bound_ctrl:1
	ds_read_b128 v[174:177], v80 offset:15104
	v_add_f32_dpp v182, v182, v182 row_ror:1 row_mask:0xf bank_mask:0xf bound_ctrl:1
	v_add_f32_dpp v183, v183, v183 row_ror:1 row_mask:0xf bank_mask:0xf bound_ctrl:1
	v_pk_mul_f32 v[240:241], v[46:47], v[182:183] op_sel_hi:[1,0]
	v_pk_mul_f32 v[242:243], v[48:49], v[182:183] op_sel_hi:[1,0]
	v_pk_mul_f32 v[244:245], v[46:47], v[182:183] op_sel:[0,1]
	v_pk_mul_f32 v[246:247], v[48:49], v[182:183] op_sel:[0,1]
	ds_write_b64 v2, v[182:183] offset:1536
	v_pk_fma_f32 v[72:73], v[72:73], v[44:45], v[242:243]
	v_pk_fma_f32 v[76:77], v[76:77], v[44:45], v[246:247]
	v_pk_fma_f32 v[70:71], v[70:71], v[42:43], v[240:241]
	v_pk_fma_f32 v[74:75], v[74:75], v[42:43], v[244:245]
	v_pk_fma_f32 v[72:73], v[52:53], v[54:55], v[72:73] op_sel_hi:[1,0,1]
	v_pk_fma_f32 v[76:77], v[52:53], v[54:55], v[76:77] op_sel:[0,1,0]
	v_pk_fma_f32 v[70:71], v[50:51], v[54:55], v[70:71] op_sel_hi:[1,0,1]
	v_pk_fma_f32 v[74:75], v[50:51], v[54:55], v[74:75] op_sel:[0,1,0]
	s_waitcnt lgkmcnt(7)
	ds_read_b64 v[54:55], v81 offset:1920
	v_pk_mul_f32 v[178:179], v[72:73], v[58:59]
	v_pk_mul_f32 v[180:181], v[76:77], v[58:59]
	v_pk_fma_f32 v[178:179], v[70:71], v[56:57], v[178:179]
	v_pk_fma_f32 v[180:181], v[74:75], v[56:57], v[180:181]
	v_add_f32_e32 v184, v178, v179
	v_add_f32_e32 v185, v180, v181
	ds_read_b128 v[38:41], v80 offset:15360
	v_add_f32_dpp v184, v184, v184 row_ror:8 row_mask:0xf bank_mask:0xf bound_ctrl:1
	v_add_f32_dpp v185, v185, v185 row_ror:8 row_mask:0xf bank_mask:0xf bound_ctrl:1
	ds_read_b128 v[42:45], v80 offset:15616
	v_add_f32_dpp v184, v184, v184 row_ror:4 row_mask:0xf bank_mask:0xf bound_ctrl:1
	v_add_f32_dpp v185, v185, v185 row_ror:4 row_mask:0xf bank_mask:0xf bound_ctrl:1
	ds_read_b128 v[46:49], v80 offset:15872
	v_add_f32_dpp v184, v184, v184 row_ror:2 row_mask:0xf bank_mask:0xf bound_ctrl:1
	v_add_f32_dpp v185, v185, v185 row_ror:2 row_mask:0xf bank_mask:0xf bound_ctrl:1
	ds_read_b128 v[50:53], v80 offset:16128
	v_add_f32_dpp v184, v184, v184 row_ror:1 row_mask:0xf bank_mask:0xf bound_ctrl:1
	v_add_f32_dpp v185, v185, v185 row_ror:1 row_mask:0xf bank_mask:0xf bound_ctrl:1
	v_pk_mul_f32 v[240:241], v[154:155], v[184:185] op_sel_hi:[1,0]
	v_pk_mul_f32 v[242:243], v[156:157], v[184:185] op_sel_hi:[1,0]
	v_pk_mul_f32 v[244:245], v[154:155], v[184:185] op_sel:[0,1]
	v_pk_mul_f32 v[246:247], v[156:157], v[184:185] op_sel:[0,1]
	ds_write_b64 v2, v[184:185] offset:1664
	v_pk_fma_f32 v[72:73], v[72:73], v[152:153], v[242:243]
	v_pk_fma_f32 v[76:77], v[76:77], v[152:153], v[246:247]
	v_pk_fma_f32 v[70:71], v[70:71], v[150:151], v[240:241]
	v_pk_fma_f32 v[74:75], v[74:75], v[150:151], v[244:245]
	v_pk_fma_f32 v[72:73], v[160:161], v[60:61], v[72:73] op_sel_hi:[1,0,1]
	v_pk_fma_f32 v[76:77], v[160:161], v[60:61], v[76:77] op_sel:[0,1,0]
	v_pk_fma_f32 v[70:71], v[158:159], v[60:61], v[70:71] op_sel_hi:[1,0,1]
	v_pk_fma_f32 v[74:75], v[158:159], v[60:61], v[74:75] op_sel:[0,1,0]
	s_waitcnt lgkmcnt(7)
	ds_read_b64 v[60:61], v81 offset:2048
	v_pk_mul_f32 v[178:179], v[72:73], v[164:165]
	v_pk_mul_f32 v[180:181], v[76:77], v[164:165]
	v_pk_fma_f32 v[178:179], v[70:71], v[162:163], v[178:179]
	v_pk_fma_f32 v[180:181], v[74:75], v[162:163], v[180:181]
	v_add_f32_e32 v182, v178, v179
	v_add_f32_e32 v183, v180, v181
	ds_read_b128 v[56:59], v80 offset:16384
	v_add_f32_dpp v182, v182, v182 row_ror:8 row_mask:0xf bank_mask:0xf bound_ctrl:1
	v_add_f32_dpp v183, v183, v183 row_ror:8 row_mask:0xf bank_mask:0xf bound_ctrl:1
	ds_read_b128 v[150:153], v80 offset:16640
	v_add_f32_dpp v182, v182, v182 row_ror:4 row_mask:0xf bank_mask:0xf bound_ctrl:1
	v_add_f32_dpp v183, v183, v183 row_ror:4 row_mask:0xf bank_mask:0xf bound_ctrl:1
	ds_read_b128 v[154:157], v80 offset:16896
	v_add_f32_dpp v182, v182, v182 row_ror:2 row_mask:0xf bank_mask:0xf bound_ctrl:1
	v_add_f32_dpp v183, v183, v183 row_ror:2 row_mask:0xf bank_mask:0xf bound_ctrl:1
	ds_read_b128 v[158:161], v80 offset:17152
	v_add_f32_dpp v182, v182, v182 row_ror:1 row_mask:0xf bank_mask:0xf bound_ctrl:1
	v_add_f32_dpp v183, v183, v183 row_ror:1 row_mask:0xf bank_mask:0xf bound_ctrl:1
	v_pk_mul_f32 v[240:241], v[170:171], v[182:183] op_sel_hi:[1,0]
	v_pk_mul_f32 v[242:243], v[172:173], v[182:183] op_sel_hi:[1,0]
	v_pk_mul_f32 v[244:245], v[170:171], v[182:183] op_sel:[0,1]
	v_pk_mul_f32 v[246:247], v[172:173], v[182:183] op_sel:[0,1]
	ds_write_b64 v2, v[182:183] offset:1792
	v_pk_fma_f32 v[72:73], v[72:73], v[168:169], v[242:243]
	v_pk_fma_f32 v[76:77], v[76:77], v[168:169], v[246:247]
	v_pk_fma_f32 v[70:71], v[70:71], v[166:167], v[240:241]
	v_pk_fma_f32 v[74:75], v[74:75], v[166:167], v[244:245]
	v_pk_fma_f32 v[72:73], v[176:177], v[78:79], v[72:73] op_sel_hi:[1,0,1]
	v_pk_fma_f32 v[76:77], v[176:177], v[78:79], v[76:77] op_sel:[0,1,0]
	v_pk_fma_f32 v[70:71], v[174:175], v[78:79], v[70:71] op_sel_hi:[1,0,1]
	v_pk_fma_f32 v[74:75], v[174:175], v[78:79], v[74:75] op_sel:[0,1,0]
	s_waitcnt lgkmcnt(7)
	ds_read_b64 v[78:79], v81 offset:2176
	v_pk_mul_f32 v[178:179], v[72:73], v[40:41]
	v_pk_mul_f32 v[180:181], v[76:77], v[40:41]
	v_pk_fma_f32 v[178:179], v[70:71], v[38:39], v[178:179]
	v_pk_fma_f32 v[180:181], v[74:75], v[38:39], v[180:181]
	v_add_f32_e32 v184, v178, v179
	v_add_f32_e32 v185, v180, v181
	ds_read_b128 v[162:165], v80 offset:17408
	v_add_f32_dpp v184, v184, v184 row_ror:8 row_mask:0xf bank_mask:0xf bound_ctrl:1
	v_add_f32_dpp v185, v185, v185 row_ror:8 row_mask:0xf bank_mask:0xf bound_ctrl:1
	ds_read_b128 v[166:169], v80 offset:17664
	v_add_f32_dpp v184, v184, v184 row_ror:4 row_mask:0xf bank_mask:0xf bound_ctrl:1
	v_add_f32_dpp v185, v185, v185 row_ror:4 row_mask:0xf bank_mask:0xf bound_ctrl:1
	ds_read_b128 v[170:173], v80 offset:17920
	v_add_f32_dpp v184, v184, v184 row_ror:2 row_mask:0xf bank_mask:0xf bound_ctrl:1
	v_add_f32_dpp v185, v185, v185 row_ror:2 row_mask:0xf bank_mask:0xf bound_ctrl:1
	ds_read_b128 v[174:177], v80 offset:18176
	v_add_f32_dpp v184, v184, v184 row_ror:1 row_mask:0xf bank_mask:0xf bound_ctrl:1
	v_add_f32_dpp v185, v185, v185 row_ror:1 row_mask:0xf bank_mask:0xf bound_ctrl:1
	v_pk_mul_f32 v[240:241], v[46:47], v[184:185] op_sel_hi:[1,0]
	v_pk_mul_f32 v[242:243], v[48:49], v[184:185] op_sel_hi:[1,0]
	v_pk_mul_f32 v[244:245], v[46:47], v[184:185] op_sel:[0,1]
	v_pk_mul_f32 v[246:247], v[48:49], v[184:185] op_sel:[0,1]
	ds_write_b64 v2, v[184:185] offset:1920
	v_pk_fma_f32 v[72:73], v[72:73], v[44:45], v[242:243]
	v_pk_fma_f32 v[76:77], v[76:77], v[44:45], v[246:247]
	v_pk_fma_f32 v[70:71], v[70:71], v[42:43], v[240:241]
	v_pk_fma_f32 v[74:75], v[74:75], v[42:43], v[244:245]
	v_pk_fma_f32 v[72:73], v[52:53], v[54:55], v[72:73] op_sel_hi:[1,0,1]
	v_pk_fma_f32 v[76:77], v[52:53], v[54:55], v[76:77] op_sel:[0,1,0]
	v_pk_fma_f32 v[70:71], v[50:51], v[54:55], v[70:71] op_sel_hi:[1,0,1]
	v_pk_fma_f32 v[74:75], v[50:51], v[54:55], v[74:75] op_sel:[0,1,0]
	s_waitcnt lgkmcnt(7)
	ds_read_b64 v[54:55], v81 offset:2304
	v_pk_mul_f32 v[178:179], v[72:73], v[58:59]
	v_pk_mul_f32 v[180:181], v[76:77], v[58:59]
	v_pk_fma_f32 v[178:179], v[70:71], v[56:57], v[178:179]
	v_pk_fma_f32 v[180:181], v[74:75], v[56:57], v[180:181]
	v_add_f32_e32 v182, v178, v179
	v_add_f32_e32 v183, v180, v181
	ds_read_b128 v[38:41], v80 offset:18432
	v_add_f32_dpp v182, v182, v182 row_ror:8 row_mask:0xf bank_mask:0xf bound_ctrl:1
	v_add_f32_dpp v183, v183, v183 row_ror:8 row_mask:0xf bank_mask:0xf bound_ctrl:1
	ds_read_b128 v[42:45], v80 offset:18688
	v_add_f32_dpp v182, v182, v182 row_ror:4 row_mask:0xf bank_mask:0xf bound_ctrl:1
	v_add_f32_dpp v183, v183, v183 row_ror:4 row_mask:0xf bank_mask:0xf bound_ctrl:1
	ds_read_b128 v[46:49], v80 offset:18944
	v_add_f32_dpp v182, v182, v182 row_ror:2 row_mask:0xf bank_mask:0xf bound_ctrl:1
	v_add_f32_dpp v183, v183, v183 row_ror:2 row_mask:0xf bank_mask:0xf bound_ctrl:1
	ds_read_b128 v[50:53], v80 offset:19200
	v_add_f32_dpp v182, v182, v182 row_ror:1 row_mask:0xf bank_mask:0xf bound_ctrl:1
	v_add_f32_dpp v183, v183, v183 row_ror:1 row_mask:0xf bank_mask:0xf bound_ctrl:1
	v_pk_mul_f32 v[240:241], v[154:155], v[182:183] op_sel_hi:[1,0]
	v_pk_mul_f32 v[242:243], v[156:157], v[182:183] op_sel_hi:[1,0]
	v_pk_mul_f32 v[244:245], v[154:155], v[182:183] op_sel:[0,1]
	v_pk_mul_f32 v[246:247], v[156:157], v[182:183] op_sel:[0,1]
	ds_write_b64 v2, v[182:183] offset:2048
	v_pk_fma_f32 v[72:73], v[72:73], v[152:153], v[242:243]
	v_pk_fma_f32 v[76:77], v[76:77], v[152:153], v[246:247]
	v_pk_fma_f32 v[70:71], v[70:71], v[150:151], v[240:241]
	v_pk_fma_f32 v[74:75], v[74:75], v[150:151], v[244:245]
	v_pk_fma_f32 v[72:73], v[160:161], v[60:61], v[72:73] op_sel_hi:[1,0,1]
	v_pk_fma_f32 v[76:77], v[160:161], v[60:61], v[76:77] op_sel:[0,1,0]
	v_pk_fma_f32 v[70:71], v[158:159], v[60:61], v[70:71] op_sel_hi:[1,0,1]
	v_pk_fma_f32 v[74:75], v[158:159], v[60:61], v[74:75] op_sel:[0,1,0]
	s_waitcnt lgkmcnt(7)
	ds_read_b64 v[60:61], v81 offset:2432
	v_pk_mul_f32 v[178:179], v[72:73], v[164:165]
	v_pk_mul_f32 v[180:181], v[76:77], v[164:165]
	v_pk_fma_f32 v[178:179], v[70:71], v[162:163], v[178:179]
	v_pk_fma_f32 v[180:181], v[74:75], v[162:163], v[180:181]
	v_add_f32_e32 v184, v178, v179
	v_add_f32_e32 v185, v180, v181
	ds_read_b128 v[56:59], v80 offset:19456
	v_add_f32_dpp v184, v184, v184 row_ror:8 row_mask:0xf bank_mask:0xf bound_ctrl:1
	v_add_f32_dpp v185, v185, v185 row_ror:8 row_mask:0xf bank_mask:0xf bound_ctrl:1
	ds_read_b128 v[150:153], v80 offset:19712
	v_add_f32_dpp v184, v184, v184 row_ror:4 row_mask:0xf bank_mask:0xf bound_ctrl:1
	v_add_f32_dpp v185, v185, v185 row_ror:4 row_mask:0xf bank_mask:0xf bound_ctrl:1
	ds_read_b128 v[154:157], v80 offset:19968
	v_add_f32_dpp v184, v184, v184 row_ror:2 row_mask:0xf bank_mask:0xf bound_ctrl:1
	v_add_f32_dpp v185, v185, v185 row_ror:2 row_mask:0xf bank_mask:0xf bound_ctrl:1
	ds_read_b128 v[158:161], v80 offset:20224
	v_add_f32_dpp v184, v184, v184 row_ror:1 row_mask:0xf bank_mask:0xf bound_ctrl:1
	v_add_f32_dpp v185, v185, v185 row_ror:1 row_mask:0xf bank_mask:0xf bound_ctrl:1
	v_pk_mul_f32 v[240:241], v[170:171], v[184:185] op_sel_hi:[1,0]
	v_pk_mul_f32 v[242:243], v[172:173], v[184:185] op_sel_hi:[1,0]
	v_pk_mul_f32 v[244:245], v[170:171], v[184:185] op_sel:[0,1]
	v_pk_mul_f32 v[246:247], v[172:173], v[184:185] op_sel:[0,1]
	ds_write_b64 v2, v[184:185] offset:2176
	v_pk_fma_f32 v[72:73], v[72:73], v[168:169], v[242:243]
	v_pk_fma_f32 v[76:77], v[76:77], v[168:169], v[246:247]
	v_pk_fma_f32 v[70:71], v[70:71], v[166:167], v[240:241]
	v_pk_fma_f32 v[74:75], v[74:75], v[166:167], v[244:245]
	v_pk_fma_f32 v[72:73], v[176:177], v[78:79], v[72:73] op_sel_hi:[1,0,1]
	v_pk_fma_f32 v[76:77], v[176:177], v[78:79], v[76:77] op_sel:[0,1,0]
	v_pk_fma_f32 v[70:71], v[174:175], v[78:79], v[70:71] op_sel_hi:[1,0,1]
	v_pk_fma_f32 v[74:75], v[174:175], v[78:79], v[74:75] op_sel:[0,1,0]
	s_waitcnt lgkmcnt(7)
	ds_read_b64 v[78:79], v81 offset:2560
	v_pk_mul_f32 v[178:179], v[72:73], v[40:41]
	v_pk_mul_f32 v[180:181], v[76:77], v[40:41]
	v_pk_fma_f32 v[178:179], v[70:71], v[38:39], v[178:179]
	v_pk_fma_f32 v[180:181], v[74:75], v[38:39], v[180:181]
	v_add_f32_e32 v182, v178, v179
	v_add_f32_e32 v183, v180, v181
	ds_read_b128 v[162:165], v80 offset:20480
	v_add_f32_dpp v182, v182, v182 row_ror:8 row_mask:0xf bank_mask:0xf bound_ctrl:1
	v_add_f32_dpp v183, v183, v183 row_ror:8 row_mask:0xf bank_mask:0xf bound_ctrl:1
	ds_read_b128 v[166:169], v80 offset:20736
	v_add_f32_dpp v182, v182, v182 row_ror:4 row_mask:0xf bank_mask:0xf bound_ctrl:1
	v_add_f32_dpp v183, v183, v183 row_ror:4 row_mask:0xf bank_mask:0xf bound_ctrl:1
	ds_read_b128 v[170:173], v80 offset:20992
	v_add_f32_dpp v182, v182, v182 row_ror:2 row_mask:0xf bank_mask:0xf bound_ctrl:1
	v_add_f32_dpp v183, v183, v183 row_ror:2 row_mask:0xf bank_mask:0xf bound_ctrl:1
	ds_read_b128 v[174:177], v80 offset:21248
	v_add_f32_dpp v182, v182, v182 row_ror:1 row_mask:0xf bank_mask:0xf bound_ctrl:1
	v_add_f32_dpp v183, v183, v183 row_ror:1 row_mask:0xf bank_mask:0xf bound_ctrl:1
	v_pk_mul_f32 v[240:241], v[46:47], v[182:183] op_sel_hi:[1,0]
	v_pk_mul_f32 v[242:243], v[48:49], v[182:183] op_sel_hi:[1,0]
	v_pk_mul_f32 v[244:245], v[46:47], v[182:183] op_sel:[0,1]
	v_pk_mul_f32 v[246:247], v[48:49], v[182:183] op_sel:[0,1]
	ds_write_b64 v2, v[182:183] offset:2304
	v_pk_fma_f32 v[72:73], v[72:73], v[44:45], v[242:243]
	v_pk_fma_f32 v[76:77], v[76:77], v[44:45], v[246:247]
	v_pk_fma_f32 v[70:71], v[70:71], v[42:43], v[240:241]
	v_pk_fma_f32 v[74:75], v[74:75], v[42:43], v[244:245]
	v_pk_fma_f32 v[72:73], v[52:53], v[54:55], v[72:73] op_sel_hi:[1,0,1]
	v_pk_fma_f32 v[76:77], v[52:53], v[54:55], v[76:77] op_sel:[0,1,0]
	v_pk_fma_f32 v[70:71], v[50:51], v[54:55], v[70:71] op_sel_hi:[1,0,1]
	v_pk_fma_f32 v[74:75], v[50:51], v[54:55], v[74:75] op_sel:[0,1,0]
	s_waitcnt lgkmcnt(7)
	ds_read_b64 v[54:55], v81 offset:2688
	v_pk_mul_f32 v[178:179], v[72:73], v[58:59]
	v_pk_mul_f32 v[180:181], v[76:77], v[58:59]
	v_pk_fma_f32 v[178:179], v[70:71], v[56:57], v[178:179]
	v_pk_fma_f32 v[180:181], v[74:75], v[56:57], v[180:181]
	v_add_f32_e32 v184, v178, v179
	v_add_f32_e32 v185, v180, v181
	ds_read_b128 v[38:41], v80 offset:21504
	v_add_f32_dpp v184, v184, v184 row_ror:8 row_mask:0xf bank_mask:0xf bound_ctrl:1
	v_add_f32_dpp v185, v185, v185 row_ror:8 row_mask:0xf bank_mask:0xf bound_ctrl:1
	ds_read_b128 v[42:45], v80 offset:21760
	v_add_f32_dpp v184, v184, v184 row_ror:4 row_mask:0xf bank_mask:0xf bound_ctrl:1
	v_add_f32_dpp v185, v185, v185 row_ror:4 row_mask:0xf bank_mask:0xf bound_ctrl:1
	ds_read_b128 v[46:49], v80 offset:22016
	v_add_f32_dpp v184, v184, v184 row_ror:2 row_mask:0xf bank_mask:0xf bound_ctrl:1
	v_add_f32_dpp v185, v185, v185 row_ror:2 row_mask:0xf bank_mask:0xf bound_ctrl:1
	ds_read_b128 v[50:53], v80 offset:22272
	v_add_f32_dpp v184, v184, v184 row_ror:1 row_mask:0xf bank_mask:0xf bound_ctrl:1
	v_add_f32_dpp v185, v185, v185 row_ror:1 row_mask:0xf bank_mask:0xf bound_ctrl:1
	v_pk_mul_f32 v[240:241], v[154:155], v[184:185] op_sel_hi:[1,0]
	v_pk_mul_f32 v[242:243], v[156:157], v[184:185] op_sel_hi:[1,0]
	v_pk_mul_f32 v[244:245], v[154:155], v[184:185] op_sel:[0,1]
	v_pk_mul_f32 v[246:247], v[156:157], v[184:185] op_sel:[0,1]
	ds_write_b64 v2, v[184:185] offset:2432
	v_pk_fma_f32 v[72:73], v[72:73], v[152:153], v[242:243]
	v_pk_fma_f32 v[76:77], v[76:77], v[152:153], v[246:247]
	v_pk_fma_f32 v[70:71], v[70:71], v[150:151], v[240:241]
	v_pk_fma_f32 v[74:75], v[74:75], v[150:151], v[244:245]
	v_pk_fma_f32 v[72:73], v[160:161], v[60:61], v[72:73] op_sel_hi:[1,0,1]
	v_pk_fma_f32 v[76:77], v[160:161], v[60:61], v[76:77] op_sel:[0,1,0]
	v_pk_fma_f32 v[70:71], v[158:159], v[60:61], v[70:71] op_sel_hi:[1,0,1]
	v_pk_fma_f32 v[74:75], v[158:159], v[60:61], v[74:75] op_sel:[0,1,0]
	s_waitcnt lgkmcnt(7)
	ds_read_b64 v[60:61], v81 offset:2816
	v_pk_mul_f32 v[178:179], v[72:73], v[164:165]
	v_pk_mul_f32 v[180:181], v[76:77], v[164:165]
	v_pk_fma_f32 v[178:179], v[70:71], v[162:163], v[178:179]
	v_pk_fma_f32 v[180:181], v[74:75], v[162:163], v[180:181]
	v_add_f32_e32 v182, v178, v179
	v_add_f32_e32 v183, v180, v181
	ds_read_b128 v[56:59], v80 offset:22528
	v_add_f32_dpp v182, v182, v182 row_ror:8 row_mask:0xf bank_mask:0xf bound_ctrl:1
	v_add_f32_dpp v183, v183, v183 row_ror:8 row_mask:0xf bank_mask:0xf bound_ctrl:1
	ds_read_b128 v[150:153], v80 offset:22784
	v_add_f32_dpp v182, v182, v182 row_ror:4 row_mask:0xf bank_mask:0xf bound_ctrl:1
	v_add_f32_dpp v183, v183, v183 row_ror:4 row_mask:0xf bank_mask:0xf bound_ctrl:1
	ds_read_b128 v[154:157], v80 offset:23040
	v_add_f32_dpp v182, v182, v182 row_ror:2 row_mask:0xf bank_mask:0xf bound_ctrl:1
	v_add_f32_dpp v183, v183, v183 row_ror:2 row_mask:0xf bank_mask:0xf bound_ctrl:1
	ds_read_b128 v[158:161], v80 offset:23296
	v_add_f32_dpp v182, v182, v182 row_ror:1 row_mask:0xf bank_mask:0xf bound_ctrl:1
	v_add_f32_dpp v183, v183, v183 row_ror:1 row_mask:0xf bank_mask:0xf bound_ctrl:1
	v_pk_mul_f32 v[240:241], v[170:171], v[182:183] op_sel_hi:[1,0]
	v_pk_mul_f32 v[242:243], v[172:173], v[182:183] op_sel_hi:[1,0]
	v_pk_mul_f32 v[244:245], v[170:171], v[182:183] op_sel:[0,1]
	v_pk_mul_f32 v[246:247], v[172:173], v[182:183] op_sel:[0,1]
	ds_write_b64 v2, v[182:183] offset:2560
	v_pk_fma_f32 v[72:73], v[72:73], v[168:169], v[242:243]
	v_pk_fma_f32 v[76:77], v[76:77], v[168:169], v[246:247]
	v_pk_fma_f32 v[70:71], v[70:71], v[166:167], v[240:241]
	v_pk_fma_f32 v[74:75], v[74:75], v[166:167], v[244:245]
	v_pk_fma_f32 v[72:73], v[176:177], v[78:79], v[72:73] op_sel_hi:[1,0,1]
	v_pk_fma_f32 v[76:77], v[176:177], v[78:79], v[76:77] op_sel:[0,1,0]
	v_pk_fma_f32 v[70:71], v[174:175], v[78:79], v[70:71] op_sel_hi:[1,0,1]
	v_pk_fma_f32 v[74:75], v[174:175], v[78:79], v[74:75] op_sel:[0,1,0]
	s_waitcnt lgkmcnt(7)
	ds_read_b64 v[78:79], v81 offset:2944
	v_pk_mul_f32 v[178:179], v[72:73], v[40:41]
	v_pk_mul_f32 v[180:181], v[76:77], v[40:41]
	v_pk_fma_f32 v[178:179], v[70:71], v[38:39], v[178:179]
	v_pk_fma_f32 v[180:181], v[74:75], v[38:39], v[180:181]
	v_add_f32_e32 v184, v178, v179
	v_add_f32_e32 v185, v180, v181
	ds_read_b128 v[162:165], v80 offset:23552
	v_add_f32_dpp v184, v184, v184 row_ror:8 row_mask:0xf bank_mask:0xf bound_ctrl:1
	v_add_f32_dpp v185, v185, v185 row_ror:8 row_mask:0xf bank_mask:0xf bound_ctrl:1
	ds_read_b128 v[166:169], v80 offset:23808
	v_add_f32_dpp v184, v184, v184 row_ror:4 row_mask:0xf bank_mask:0xf bound_ctrl:1
	v_add_f32_dpp v185, v185, v185 row_ror:4 row_mask:0xf bank_mask:0xf bound_ctrl:1
	ds_read_b128 v[170:173], v80 offset:24064
	v_add_f32_dpp v184, v184, v184 row_ror:2 row_mask:0xf bank_mask:0xf bound_ctrl:1
	v_add_f32_dpp v185, v185, v185 row_ror:2 row_mask:0xf bank_mask:0xf bound_ctrl:1
	ds_read_b128 v[174:177], v80 offset:24320
	v_add_f32_dpp v184, v184, v184 row_ror:1 row_mask:0xf bank_mask:0xf bound_ctrl:1
	v_add_f32_dpp v185, v185, v185 row_ror:1 row_mask:0xf bank_mask:0xf bound_ctrl:1
	v_pk_mul_f32 v[240:241], v[46:47], v[184:185] op_sel_hi:[1,0]
	v_pk_mul_f32 v[242:243], v[48:49], v[184:185] op_sel_hi:[1,0]
	v_pk_mul_f32 v[244:245], v[46:47], v[184:185] op_sel:[0,1]
	v_pk_mul_f32 v[246:247], v[48:49], v[184:185] op_sel:[0,1]
	ds_write_b64 v2, v[184:185] offset:2688
	v_pk_fma_f32 v[72:73], v[72:73], v[44:45], v[242:243]
	v_pk_fma_f32 v[76:77], v[76:77], v[44:45], v[246:247]
	v_pk_fma_f32 v[70:71], v[70:71], v[42:43], v[240:241]
	v_pk_fma_f32 v[74:75], v[74:75], v[42:43], v[244:245]
	v_pk_fma_f32 v[72:73], v[52:53], v[54:55], v[72:73] op_sel_hi:[1,0,1]
	v_pk_fma_f32 v[76:77], v[52:53], v[54:55], v[76:77] op_sel:[0,1,0]
	v_pk_fma_f32 v[70:71], v[50:51], v[54:55], v[70:71] op_sel_hi:[1,0,1]
	v_pk_fma_f32 v[74:75], v[50:51], v[54:55], v[74:75] op_sel:[0,1,0]
	s_waitcnt lgkmcnt(7)
	ds_read_b64 v[54:55], v81 offset:3072
	v_pk_mul_f32 v[178:179], v[72:73], v[58:59]
	v_pk_mul_f32 v[180:181], v[76:77], v[58:59]
	v_pk_fma_f32 v[178:179], v[70:71], v[56:57], v[178:179]
	v_pk_fma_f32 v[180:181], v[74:75], v[56:57], v[180:181]
	v_add_f32_e32 v182, v178, v179
	v_add_f32_e32 v183, v180, v181
	ds_read_b128 v[38:41], v80 offset:24576
	v_add_f32_dpp v182, v182, v182 row_ror:8 row_mask:0xf bank_mask:0xf bound_ctrl:1
	v_add_f32_dpp v183, v183, v183 row_ror:8 row_mask:0xf bank_mask:0xf bound_ctrl:1
	ds_read_b128 v[42:45], v80 offset:24832
	v_add_f32_dpp v182, v182, v182 row_ror:4 row_mask:0xf bank_mask:0xf bound_ctrl:1
	v_add_f32_dpp v183, v183, v183 row_ror:4 row_mask:0xf bank_mask:0xf bound_ctrl:1
	ds_read_b128 v[46:49], v80 offset:25088
	v_add_f32_dpp v182, v182, v182 row_ror:2 row_mask:0xf bank_mask:0xf bound_ctrl:1
	v_add_f32_dpp v183, v183, v183 row_ror:2 row_mask:0xf bank_mask:0xf bound_ctrl:1
	ds_read_b128 v[50:53], v80 offset:25344
	v_add_f32_dpp v182, v182, v182 row_ror:1 row_mask:0xf bank_mask:0xf bound_ctrl:1
	v_add_f32_dpp v183, v183, v183 row_ror:1 row_mask:0xf bank_mask:0xf bound_ctrl:1
	v_pk_mul_f32 v[240:241], v[154:155], v[182:183] op_sel_hi:[1,0]
	v_pk_mul_f32 v[242:243], v[156:157], v[182:183] op_sel_hi:[1,0]
	v_pk_mul_f32 v[244:245], v[154:155], v[182:183] op_sel:[0,1]
	v_pk_mul_f32 v[246:247], v[156:157], v[182:183] op_sel:[0,1]
	ds_write_b64 v2, v[182:183] offset:2816
	v_pk_fma_f32 v[72:73], v[72:73], v[152:153], v[242:243]
	v_pk_fma_f32 v[76:77], v[76:77], v[152:153], v[246:247]
	v_pk_fma_f32 v[70:71], v[70:71], v[150:151], v[240:241]
	v_pk_fma_f32 v[74:75], v[74:75], v[150:151], v[244:245]
	v_pk_fma_f32 v[72:73], v[160:161], v[60:61], v[72:73] op_sel_hi:[1,0,1]
	v_pk_fma_f32 v[76:77], v[160:161], v[60:61], v[76:77] op_sel:[0,1,0]
	v_pk_fma_f32 v[70:71], v[158:159], v[60:61], v[70:71] op_sel_hi:[1,0,1]
	v_pk_fma_f32 v[74:75], v[158:159], v[60:61], v[74:75] op_sel:[0,1,0]
	s_waitcnt lgkmcnt(7)
	ds_read_b64 v[60:61], v81 offset:3200
	v_pk_mul_f32 v[178:179], v[72:73], v[164:165]
	v_pk_mul_f32 v[180:181], v[76:77], v[164:165]
	v_pk_fma_f32 v[178:179], v[70:71], v[162:163], v[178:179]
	v_pk_fma_f32 v[180:181], v[74:75], v[162:163], v[180:181]
	v_add_f32_e32 v184, v178, v179
	v_add_f32_e32 v185, v180, v181
	ds_read_b128 v[56:59], v80 offset:25600
	v_add_f32_dpp v184, v184, v184 row_ror:8 row_mask:0xf bank_mask:0xf bound_ctrl:1
	v_add_f32_dpp v185, v185, v185 row_ror:8 row_mask:0xf bank_mask:0xf bound_ctrl:1
	ds_read_b128 v[150:153], v80 offset:25856
	v_add_f32_dpp v184, v184, v184 row_ror:4 row_mask:0xf bank_mask:0xf bound_ctrl:1
	v_add_f32_dpp v185, v185, v185 row_ror:4 row_mask:0xf bank_mask:0xf bound_ctrl:1
	ds_read_b128 v[154:157], v80 offset:26112
	v_add_f32_dpp v184, v184, v184 row_ror:2 row_mask:0xf bank_mask:0xf bound_ctrl:1
	v_add_f32_dpp v185, v185, v185 row_ror:2 row_mask:0xf bank_mask:0xf bound_ctrl:1
	ds_read_b128 v[158:161], v80 offset:26368
	v_add_f32_dpp v184, v184, v184 row_ror:1 row_mask:0xf bank_mask:0xf bound_ctrl:1
	v_add_f32_dpp v185, v185, v185 row_ror:1 row_mask:0xf bank_mask:0xf bound_ctrl:1
	v_pk_mul_f32 v[240:241], v[170:171], v[184:185] op_sel_hi:[1,0]
	v_pk_mul_f32 v[242:243], v[172:173], v[184:185] op_sel_hi:[1,0]
	v_pk_mul_f32 v[244:245], v[170:171], v[184:185] op_sel:[0,1]
	v_pk_mul_f32 v[246:247], v[172:173], v[184:185] op_sel:[0,1]
	ds_write_b64 v2, v[184:185] offset:2944
	v_pk_fma_f32 v[72:73], v[72:73], v[168:169], v[242:243]
	v_pk_fma_f32 v[76:77], v[76:77], v[168:169], v[246:247]
	v_pk_fma_f32 v[70:71], v[70:71], v[166:167], v[240:241]
	v_pk_fma_f32 v[74:75], v[74:75], v[166:167], v[244:245]
	v_pk_fma_f32 v[72:73], v[176:177], v[78:79], v[72:73] op_sel_hi:[1,0,1]
	v_pk_fma_f32 v[76:77], v[176:177], v[78:79], v[76:77] op_sel:[0,1,0]
	v_pk_fma_f32 v[70:71], v[174:175], v[78:79], v[70:71] op_sel_hi:[1,0,1]
	v_pk_fma_f32 v[74:75], v[174:175], v[78:79], v[74:75] op_sel:[0,1,0]
	s_waitcnt lgkmcnt(7)
	ds_read_b64 v[78:79], v81 offset:3328
	v_pk_mul_f32 v[178:179], v[72:73], v[40:41]
	v_pk_mul_f32 v[180:181], v[76:77], v[40:41]
	v_pk_fma_f32 v[178:179], v[70:71], v[38:39], v[178:179]
	v_pk_fma_f32 v[180:181], v[74:75], v[38:39], v[180:181]
	v_add_f32_e32 v182, v178, v179
	v_add_f32_e32 v183, v180, v181
	ds_read_b128 v[162:165], v80 offset:26624
	v_add_f32_dpp v182, v182, v182 row_ror:8 row_mask:0xf bank_mask:0xf bound_ctrl:1
	v_add_f32_dpp v183, v183, v183 row_ror:8 row_mask:0xf bank_mask:0xf bound_ctrl:1
	ds_read_b128 v[166:169], v80 offset:26880
	v_add_f32_dpp v182, v182, v182 row_ror:4 row_mask:0xf bank_mask:0xf bound_ctrl:1
	v_add_f32_dpp v183, v183, v183 row_ror:4 row_mask:0xf bank_mask:0xf bound_ctrl:1
	ds_read_b128 v[170:173], v80 offset:27136
	v_add_f32_dpp v182, v182, v182 row_ror:2 row_mask:0xf bank_mask:0xf bound_ctrl:1
	v_add_f32_dpp v183, v183, v183 row_ror:2 row_mask:0xf bank_mask:0xf bound_ctrl:1
	ds_read_b128 v[174:177], v80 offset:27392
	v_add_f32_dpp v182, v182, v182 row_ror:1 row_mask:0xf bank_mask:0xf bound_ctrl:1
	v_add_f32_dpp v183, v183, v183 row_ror:1 row_mask:0xf bank_mask:0xf bound_ctrl:1
	v_pk_mul_f32 v[240:241], v[46:47], v[182:183] op_sel_hi:[1,0]
	v_pk_mul_f32 v[242:243], v[48:49], v[182:183] op_sel_hi:[1,0]
	v_pk_mul_f32 v[244:245], v[46:47], v[182:183] op_sel:[0,1]
	v_pk_mul_f32 v[246:247], v[48:49], v[182:183] op_sel:[0,1]
	ds_write_b64 v2, v[182:183] offset:3072
	v_pk_fma_f32 v[72:73], v[72:73], v[44:45], v[242:243]
	v_pk_fma_f32 v[76:77], v[76:77], v[44:45], v[246:247]
	v_pk_fma_f32 v[70:71], v[70:71], v[42:43], v[240:241]
	v_pk_fma_f32 v[74:75], v[74:75], v[42:43], v[244:245]
	v_pk_fma_f32 v[72:73], v[52:53], v[54:55], v[72:73] op_sel_hi:[1,0,1]
	v_pk_fma_f32 v[76:77], v[52:53], v[54:55], v[76:77] op_sel:[0,1,0]
	v_pk_fma_f32 v[70:71], v[50:51], v[54:55], v[70:71] op_sel_hi:[1,0,1]
	v_pk_fma_f32 v[74:75], v[50:51], v[54:55], v[74:75] op_sel:[0,1,0]
	s_waitcnt lgkmcnt(7)
	ds_read_b64 v[54:55], v81 offset:3456
	v_pk_mul_f32 v[178:179], v[72:73], v[58:59]
	v_pk_mul_f32 v[180:181], v[76:77], v[58:59]
	v_pk_fma_f32 v[178:179], v[70:71], v[56:57], v[178:179]
	v_pk_fma_f32 v[180:181], v[74:75], v[56:57], v[180:181]
	v_add_f32_e32 v184, v178, v179
	v_add_f32_e32 v185, v180, v181
	ds_read_b128 v[38:41], v80 offset:27648
	v_add_f32_dpp v184, v184, v184 row_ror:8 row_mask:0xf bank_mask:0xf bound_ctrl:1
	v_add_f32_dpp v185, v185, v185 row_ror:8 row_mask:0xf bank_mask:0xf bound_ctrl:1
	ds_read_b128 v[42:45], v80 offset:27904
	v_add_f32_dpp v184, v184, v184 row_ror:4 row_mask:0xf bank_mask:0xf bound_ctrl:1
	v_add_f32_dpp v185, v185, v185 row_ror:4 row_mask:0xf bank_mask:0xf bound_ctrl:1
	ds_read_b128 v[46:49], v80 offset:28160
	v_add_f32_dpp v184, v184, v184 row_ror:2 row_mask:0xf bank_mask:0xf bound_ctrl:1
	v_add_f32_dpp v185, v185, v185 row_ror:2 row_mask:0xf bank_mask:0xf bound_ctrl:1
	ds_read_b128 v[50:53], v80 offset:28416
	v_add_f32_dpp v184, v184, v184 row_ror:1 row_mask:0xf bank_mask:0xf bound_ctrl:1
	v_add_f32_dpp v185, v185, v185 row_ror:1 row_mask:0xf bank_mask:0xf bound_ctrl:1
	v_pk_mul_f32 v[240:241], v[154:155], v[184:185] op_sel_hi:[1,0]
	v_pk_mul_f32 v[242:243], v[156:157], v[184:185] op_sel_hi:[1,0]
	v_pk_mul_f32 v[244:245], v[154:155], v[184:185] op_sel:[0,1]
	v_pk_mul_f32 v[246:247], v[156:157], v[184:185] op_sel:[0,1]
	ds_write_b64 v2, v[184:185] offset:3200
	v_pk_fma_f32 v[72:73], v[72:73], v[152:153], v[242:243]
	v_pk_fma_f32 v[76:77], v[76:77], v[152:153], v[246:247]
	v_pk_fma_f32 v[70:71], v[70:71], v[150:151], v[240:241]
	v_pk_fma_f32 v[74:75], v[74:75], v[150:151], v[244:245]
	v_pk_fma_f32 v[72:73], v[160:161], v[60:61], v[72:73] op_sel_hi:[1,0,1]
	v_pk_fma_f32 v[76:77], v[160:161], v[60:61], v[76:77] op_sel:[0,1,0]
	v_pk_fma_f32 v[70:71], v[158:159], v[60:61], v[70:71] op_sel_hi:[1,0,1]
	v_pk_fma_f32 v[74:75], v[158:159], v[60:61], v[74:75] op_sel:[0,1,0]
	s_waitcnt lgkmcnt(7)
	ds_read_b64 v[60:61], v81 offset:3584
	v_pk_mul_f32 v[178:179], v[72:73], v[164:165]
	v_pk_mul_f32 v[180:181], v[76:77], v[164:165]
	v_pk_fma_f32 v[178:179], v[70:71], v[162:163], v[178:179]
	v_pk_fma_f32 v[180:181], v[74:75], v[162:163], v[180:181]
	v_add_f32_e32 v182, v178, v179
	v_add_f32_e32 v183, v180, v181
	ds_read_b128 v[56:59], v80 offset:28672
	v_add_f32_dpp v182, v182, v182 row_ror:8 row_mask:0xf bank_mask:0xf bound_ctrl:1
	v_add_f32_dpp v183, v183, v183 row_ror:8 row_mask:0xf bank_mask:0xf bound_ctrl:1
	ds_read_b128 v[150:153], v80 offset:28928
	v_add_f32_dpp v182, v182, v182 row_ror:4 row_mask:0xf bank_mask:0xf bound_ctrl:1
	v_add_f32_dpp v183, v183, v183 row_ror:4 row_mask:0xf bank_mask:0xf bound_ctrl:1
	ds_read_b128 v[154:157], v80 offset:29184
	v_add_f32_dpp v182, v182, v182 row_ror:2 row_mask:0xf bank_mask:0xf bound_ctrl:1
	v_add_f32_dpp v183, v183, v183 row_ror:2 row_mask:0xf bank_mask:0xf bound_ctrl:1
	ds_read_b128 v[158:161], v80 offset:29440
	v_add_f32_dpp v182, v182, v182 row_ror:1 row_mask:0xf bank_mask:0xf bound_ctrl:1
	v_add_f32_dpp v183, v183, v183 row_ror:1 row_mask:0xf bank_mask:0xf bound_ctrl:1
	v_pk_mul_f32 v[240:241], v[170:171], v[182:183] op_sel_hi:[1,0]
	v_pk_mul_f32 v[242:243], v[172:173], v[182:183] op_sel_hi:[1,0]
	v_pk_mul_f32 v[244:245], v[170:171], v[182:183] op_sel:[0,1]
	v_pk_mul_f32 v[246:247], v[172:173], v[182:183] op_sel:[0,1]
	ds_write_b64 v2, v[182:183] offset:3328
	v_pk_fma_f32 v[72:73], v[72:73], v[168:169], v[242:243]
	v_pk_fma_f32 v[76:77], v[76:77], v[168:169], v[246:247]
	v_pk_fma_f32 v[70:71], v[70:71], v[166:167], v[240:241]
	v_pk_fma_f32 v[74:75], v[74:75], v[166:167], v[244:245]
	v_pk_fma_f32 v[72:73], v[176:177], v[78:79], v[72:73] op_sel_hi:[1,0,1]
	v_pk_fma_f32 v[76:77], v[176:177], v[78:79], v[76:77] op_sel:[0,1,0]
	v_pk_fma_f32 v[70:71], v[174:175], v[78:79], v[70:71] op_sel_hi:[1,0,1]
	v_pk_fma_f32 v[74:75], v[174:175], v[78:79], v[74:75] op_sel:[0,1,0]
	s_waitcnt lgkmcnt(7)
	ds_read_b64 v[78:79], v81 offset:3712
	v_pk_mul_f32 v[178:179], v[72:73], v[40:41]
	v_pk_mul_f32 v[180:181], v[76:77], v[40:41]
	v_pk_fma_f32 v[178:179], v[70:71], v[38:39], v[178:179]
	v_pk_fma_f32 v[180:181], v[74:75], v[38:39], v[180:181]
	v_add_f32_e32 v184, v178, v179
	v_add_f32_e32 v185, v180, v181
	ds_read_b128 v[162:165], v80 offset:29696
	v_add_f32_dpp v184, v184, v184 row_ror:8 row_mask:0xf bank_mask:0xf bound_ctrl:1
	v_add_f32_dpp v185, v185, v185 row_ror:8 row_mask:0xf bank_mask:0xf bound_ctrl:1
	ds_read_b128 v[166:169], v80 offset:29952
	v_add_f32_dpp v184, v184, v184 row_ror:4 row_mask:0xf bank_mask:0xf bound_ctrl:1
	v_add_f32_dpp v185, v185, v185 row_ror:4 row_mask:0xf bank_mask:0xf bound_ctrl:1
	ds_read_b128 v[170:173], v80 offset:30208
	v_add_f32_dpp v184, v184, v184 row_ror:2 row_mask:0xf bank_mask:0xf bound_ctrl:1
	v_add_f32_dpp v185, v185, v185 row_ror:2 row_mask:0xf bank_mask:0xf bound_ctrl:1
	ds_read_b128 v[174:177], v80 offset:30464
	v_add_f32_dpp v184, v184, v184 row_ror:1 row_mask:0xf bank_mask:0xf bound_ctrl:1
	v_add_f32_dpp v185, v185, v185 row_ror:1 row_mask:0xf bank_mask:0xf bound_ctrl:1
	v_pk_mul_f32 v[240:241], v[46:47], v[184:185] op_sel_hi:[1,0]
	v_pk_mul_f32 v[242:243], v[48:49], v[184:185] op_sel_hi:[1,0]
	v_pk_mul_f32 v[244:245], v[46:47], v[184:185] op_sel:[0,1]
	v_pk_mul_f32 v[246:247], v[48:49], v[184:185] op_sel:[0,1]
	ds_write_b64 v2, v[184:185] offset:3456
	v_pk_fma_f32 v[72:73], v[72:73], v[44:45], v[242:243]
	v_pk_fma_f32 v[76:77], v[76:77], v[44:45], v[246:247]
	v_pk_fma_f32 v[70:71], v[70:71], v[42:43], v[240:241]
	v_pk_fma_f32 v[74:75], v[74:75], v[42:43], v[244:245]
	v_pk_fma_f32 v[72:73], v[52:53], v[54:55], v[72:73] op_sel_hi:[1,0,1]
	v_pk_fma_f32 v[76:77], v[52:53], v[54:55], v[76:77] op_sel:[0,1,0]
	v_pk_fma_f32 v[70:71], v[50:51], v[54:55], v[70:71] op_sel_hi:[1,0,1]
	v_pk_fma_f32 v[74:75], v[50:51], v[54:55], v[74:75] op_sel:[0,1,0]
	s_waitcnt lgkmcnt(7)
	ds_read_b64 v[54:55], v81 offset:3840
	v_pk_mul_f32 v[178:179], v[72:73], v[58:59]
	v_pk_mul_f32 v[180:181], v[76:77], v[58:59]
	v_pk_fma_f32 v[178:179], v[70:71], v[56:57], v[178:179]
	v_pk_fma_f32 v[180:181], v[74:75], v[56:57], v[180:181]
	v_add_f32_e32 v182, v178, v179
	v_add_f32_e32 v183, v180, v181
	ds_read_b128 v[38:41], v80 offset:30720
	v_add_f32_dpp v182, v182, v182 row_ror:8 row_mask:0xf bank_mask:0xf bound_ctrl:1
	v_add_f32_dpp v183, v183, v183 row_ror:8 row_mask:0xf bank_mask:0xf bound_ctrl:1
	ds_read_b128 v[42:45], v80 offset:30976
	v_add_f32_dpp v182, v182, v182 row_ror:4 row_mask:0xf bank_mask:0xf bound_ctrl:1
	v_add_f32_dpp v183, v183, v183 row_ror:4 row_mask:0xf bank_mask:0xf bound_ctrl:1
	ds_read_b128 v[46:49], v80 offset:31232
	v_add_f32_dpp v182, v182, v182 row_ror:2 row_mask:0xf bank_mask:0xf bound_ctrl:1
	v_add_f32_dpp v183, v183, v183 row_ror:2 row_mask:0xf bank_mask:0xf bound_ctrl:1
	ds_read_b128 v[50:53], v80 offset:31488
	v_add_f32_dpp v182, v182, v182 row_ror:1 row_mask:0xf bank_mask:0xf bound_ctrl:1
	v_add_f32_dpp v183, v183, v183 row_ror:1 row_mask:0xf bank_mask:0xf bound_ctrl:1
	v_pk_mul_f32 v[240:241], v[154:155], v[182:183] op_sel_hi:[1,0]
	v_pk_mul_f32 v[242:243], v[156:157], v[182:183] op_sel_hi:[1,0]
	v_pk_mul_f32 v[244:245], v[154:155], v[182:183] op_sel:[0,1]
	v_pk_mul_f32 v[246:247], v[156:157], v[182:183] op_sel:[0,1]
	ds_write_b64 v2, v[182:183] offset:3584
	v_pk_fma_f32 v[72:73], v[72:73], v[152:153], v[242:243]
	v_pk_fma_f32 v[76:77], v[76:77], v[152:153], v[246:247]
	v_pk_fma_f32 v[70:71], v[70:71], v[150:151], v[240:241]
	v_pk_fma_f32 v[74:75], v[74:75], v[150:151], v[244:245]
	v_pk_fma_f32 v[72:73], v[160:161], v[60:61], v[72:73] op_sel_hi:[1,0,1]
	v_pk_fma_f32 v[76:77], v[160:161], v[60:61], v[76:77] op_sel:[0,1,0]
	v_pk_fma_f32 v[70:71], v[158:159], v[60:61], v[70:71] op_sel_hi:[1,0,1]
	v_pk_fma_f32 v[74:75], v[158:159], v[60:61], v[74:75] op_sel:[0,1,0]
	s_waitcnt lgkmcnt(7)
	ds_read_b64 v[60:61], v81 offset:3968
	v_pk_mul_f32 v[178:179], v[72:73], v[164:165]
	v_pk_mul_f32 v[180:181], v[76:77], v[164:165]
	v_pk_fma_f32 v[178:179], v[70:71], v[162:163], v[178:179]
	v_pk_fma_f32 v[180:181], v[74:75], v[162:163], v[180:181]
	v_add_f32_e32 v184, v178, v179
	v_add_f32_e32 v185, v180, v181
	ds_read_b128 v[56:59], v80 offset:31744
	v_add_f32_dpp v184, v184, v184 row_ror:8 row_mask:0xf bank_mask:0xf bound_ctrl:1
	v_add_f32_dpp v185, v185, v185 row_ror:8 row_mask:0xf bank_mask:0xf bound_ctrl:1
	ds_read_b128 v[150:153], v80 offset:32000
	v_add_f32_dpp v184, v184, v184 row_ror:4 row_mask:0xf bank_mask:0xf bound_ctrl:1
	v_add_f32_dpp v185, v185, v185 row_ror:4 row_mask:0xf bank_mask:0xf bound_ctrl:1
	ds_read_b128 v[154:157], v80 offset:32256
	v_add_f32_dpp v184, v184, v184 row_ror:2 row_mask:0xf bank_mask:0xf bound_ctrl:1
	v_add_f32_dpp v185, v185, v185 row_ror:2 row_mask:0xf bank_mask:0xf bound_ctrl:1
	ds_read_b128 v[158:161], v80 offset:32512
	v_add_f32_dpp v184, v184, v184 row_ror:1 row_mask:0xf bank_mask:0xf bound_ctrl:1
	v_add_f32_dpp v185, v185, v185 row_ror:1 row_mask:0xf bank_mask:0xf bound_ctrl:1
	v_pk_mul_f32 v[240:241], v[170:171], v[184:185] op_sel_hi:[1,0]
	v_pk_mul_f32 v[242:243], v[172:173], v[184:185] op_sel_hi:[1,0]
	v_pk_mul_f32 v[244:245], v[170:171], v[184:185] op_sel:[0,1]
	v_pk_mul_f32 v[246:247], v[172:173], v[184:185] op_sel:[0,1]
	ds_write_b64 v2, v[184:185] offset:3712
	v_pk_fma_f32 v[72:73], v[72:73], v[168:169], v[242:243]
	v_pk_fma_f32 v[76:77], v[76:77], v[168:169], v[246:247]
	v_pk_fma_f32 v[70:71], v[70:71], v[166:167], v[240:241]
	v_pk_fma_f32 v[74:75], v[74:75], v[166:167], v[244:245]
	v_pk_fma_f32 v[72:73], v[176:177], v[78:79], v[72:73] op_sel_hi:[1,0,1]
	v_pk_fma_f32 v[76:77], v[176:177], v[78:79], v[76:77] op_sel:[0,1,0]
	v_pk_fma_f32 v[70:71], v[174:175], v[78:79], v[70:71] op_sel_hi:[1,0,1]
	v_pk_fma_f32 v[74:75], v[174:175], v[78:79], v[74:75] op_sel:[0,1,0]
	s_waitcnt lgkmcnt(7)
	v_pk_mul_f32 v[178:179], v[72:73], v[40:41]
	v_pk_mul_f32 v[180:181], v[76:77], v[40:41]
	v_pk_fma_f32 v[178:179], v[70:71], v[38:39], v[178:179]
	v_pk_fma_f32 v[180:181], v[74:75], v[38:39], v[180:181]
	v_add_f32_e32 v182, v178, v179
	v_add_f32_e32 v183, v180, v181
	s_nop 0
	v_add_f32_dpp v182, v182, v182 row_ror:8 row_mask:0xf bank_mask:0xf bound_ctrl:1
	v_add_f32_dpp v183, v183, v183 row_ror:8 row_mask:0xf bank_mask:0xf bound_ctrl:1
	s_nop 0
	v_add_f32_dpp v182, v182, v182 row_ror:4 row_mask:0xf bank_mask:0xf bound_ctrl:1
	v_add_f32_dpp v183, v183, v183 row_ror:4 row_mask:0xf bank_mask:0xf bound_ctrl:1
	s_nop 0
	v_add_f32_dpp v182, v182, v182 row_ror:2 row_mask:0xf bank_mask:0xf bound_ctrl:1
	v_add_f32_dpp v183, v183, v183 row_ror:2 row_mask:0xf bank_mask:0xf bound_ctrl:1
	s_nop 0
	v_add_f32_dpp v182, v182, v182 row_ror:1 row_mask:0xf bank_mask:0xf bound_ctrl:1
	v_add_f32_dpp v183, v183, v183 row_ror:1 row_mask:0xf bank_mask:0xf bound_ctrl:1
	v_pk_mul_f32 v[240:241], v[46:47], v[182:183] op_sel_hi:[1,0]
	v_pk_mul_f32 v[242:243], v[48:49], v[182:183] op_sel_hi:[1,0]
	v_pk_mul_f32 v[244:245], v[46:47], v[182:183] op_sel:[0,1]
	v_pk_mul_f32 v[246:247], v[48:49], v[182:183] op_sel:[0,1]
	ds_write_b64 v2, v[182:183] offset:3840
	v_pk_fma_f32 v[72:73], v[72:73], v[44:45], v[242:243]
	v_pk_fma_f32 v[76:77], v[76:77], v[44:45], v[246:247]
	v_pk_fma_f32 v[70:71], v[70:71], v[42:43], v[240:241]
	v_pk_fma_f32 v[74:75], v[74:75], v[42:43], v[244:245]
	v_pk_fma_f32 v[72:73], v[52:53], v[54:55], v[72:73] op_sel_hi:[1,0,1]
	v_pk_fma_f32 v[76:77], v[52:53], v[54:55], v[76:77] op_sel:[0,1,0]
	v_pk_fma_f32 v[70:71], v[50:51], v[54:55], v[70:71] op_sel_hi:[1,0,1]
	v_pk_fma_f32 v[74:75], v[50:51], v[54:55], v[74:75] op_sel:[0,1,0]
	s_waitcnt lgkmcnt(2)
	v_pk_mul_f32 v[178:179], v[72:73], v[58:59]
	v_pk_mul_f32 v[180:181], v[76:77], v[58:59]
	v_pk_fma_f32 v[178:179], v[70:71], v[56:57], v[178:179]
	v_pk_fma_f32 v[180:181], v[74:75], v[56:57], v[180:181]
	v_add_f32_e32 v184, v178, v179
	v_add_f32_e32 v185, v180, v181
	s_nop 0
	v_add_f32_dpp v184, v184, v184 row_ror:8 row_mask:0xf bank_mask:0xf bound_ctrl:1
	v_add_f32_dpp v185, v185, v185 row_ror:8 row_mask:0xf bank_mask:0xf bound_ctrl:1
	s_nop 0
	v_add_f32_dpp v184, v184, v184 row_ror:4 row_mask:0xf bank_mask:0xf bound_ctrl:1
	v_add_f32_dpp v185, v185, v185 row_ror:4 row_mask:0xf bank_mask:0xf bound_ctrl:1
	s_nop 0
	v_add_f32_dpp v184, v184, v184 row_ror:2 row_mask:0xf bank_mask:0xf bound_ctrl:1
	v_add_f32_dpp v185, v185, v185 row_ror:2 row_mask:0xf bank_mask:0xf bound_ctrl:1
	s_nop 0
	v_add_f32_dpp v184, v184, v184 row_ror:1 row_mask:0xf bank_mask:0xf bound_ctrl:1
	v_add_f32_dpp v185, v185, v185 row_ror:1 row_mask:0xf bank_mask:0xf bound_ctrl:1
	v_pk_mul_f32 v[240:241], v[154:155], v[184:185] op_sel_hi:[1,0]
	v_pk_mul_f32 v[242:243], v[156:157], v[184:185] op_sel_hi:[1,0]
	v_pk_mul_f32 v[244:245], v[154:155], v[184:185] op_sel:[0,1]
	v_pk_mul_f32 v[246:247], v[156:157], v[184:185] op_sel:[0,1]
	ds_write_b64 v2, v[184:185] offset:3968
	v_pk_fma_f32 v[72:73], v[72:73], v[152:153], v[242:243]
	v_pk_fma_f32 v[76:77], v[76:77], v[152:153], v[246:247]
	v_pk_fma_f32 v[70:71], v[70:71], v[150:151], v[240:241]
	v_pk_fma_f32 v[74:75], v[74:75], v[150:151], v[244:245]
	v_pk_fma_f32 v[72:73], v[160:161], v[60:61], v[72:73] op_sel_hi:[1,0,1]
	v_pk_fma_f32 v[76:77], v[160:161], v[60:61], v[76:77] op_sel:[0,1,0]
	v_pk_fma_f32 v[70:71], v[158:159], v[60:61], v[70:71] op_sel_hi:[1,0,1]
	v_pk_fma_f32 v[74:75], v[158:159], v[60:61], v[74:75] op_sel:[0,1,0]
	s_setprio 0
	s_branch .LBB0_483
